# P4 conversion fill replaced by the hand-written block with two tiles of loads in flight per wave
# baseline (speedup 1.0000x reference)
; __device__ __forceinline__ void conv8_fill(const Ctx& X, int base, int rank, int nblk, int n) { conv8b_run(X, (base >> 3) + rank, nblk, n); }
; #define SEAM(k) do { if (IN(k) && IN((k) + 1)) xcd_barrier(bar); } while (0)
; __device__ __forceinline__ Cvb conv8b_dec(const Ctx& X, int bit) { Cvb c; int kb, nb;
;     if (bit < I_GU8 / 8) { const int e = bit >> 8, r = bit & 255; kb = r >> 4; nb = r & 15; c.N = 2 * DFF; c.W = XP_w_gu(X) + (size_t)e * D * (2 * DFF); c.WT = XP_WguT(X) + (size_t)e * 16 * PAN_GU + (size_t)kb * PAN_GU; }
;     else { const int b2 = bit - I_GU8 / 8, e = b2 >> 7, r = b2 & 127; kb = r >> 3; nb = r & 7; c.N = D; c.W = XP_w_d(X) + (size_t)e * DFF * D; c.WT = XP_WdT(X) + (size_t)e * 16 * PAN_D + (size_t)kb * PAN_D; }
;     c.W += (size_t)(kb * 128 + 16 * X.wave) * c.N + nb * 256 + 4 * X.lane;
;     c.WT += (size_t)(nb * 256 + 32 * X.wave + (X.lane >> 3)) * 128 + 16 * (X.lane & 7);
;     return c; }
; __device__ __forceinline__ void conv8b_run(const Ctx& X, int first, int step, int count) {
;     if (count <= 0) return;
;     f32x4 v[16];
;     Cvb c = conv8b_dec(X, first), cn = c;
; #pragma unroll
;     for (int i = 0; i < 16; ++i) v[i] = __builtin_nontemporal_load((const f32x4*)(c.W + (size_t)i * c.N));
; __global__ void __launch_bounds__(NTHR, 2) fwd(Args args) {
;     ...
;         if (X.G == 256 && X.bid >= 128) conv8_fill(X, FILL_B4, X.bid - 128, FILL_W4 / NWAVES, FILL_N4); } SEAM(4);
.LBB0_661:
	s_waitcnt lgkmcnt(0)
	s_cmpk_eq_i32 s92, 0x100
	v_readlane_b32 s87, v248, 9
	s_load_dwordx2 s[94:95], s[0:1], 0xa8
	s_cselect_b64 s[2:3], -1, 0
	s_cmpk_gt_i32 s87, 0x7f
	s_cselect_b64 s[4:5], -1, 0
	s_and_b64 s[2:3], s[4:5], s[2:3]
	v_readlane_b32 s96, v248, 7
	v_readlane_b32 s64, v248, 10
	v_readlane_b32 s30, v248, 5
	s_and_b64 vcc, exec, s[2:3]
	v_readlane_b32 s97, v248, 8
	v_readlane_b32 s61, v248, 2
	v_readlane_b32 s62, v248, 3
	v_readlane_b32 s65, v248, 11
	v_readlane_b32 s31, v248, 6
	s_cbranch_vccz .LBB0_671
	s_load_dwordx2 s[6:7], s[0:1], 0x70
	s_load_dwordx2 s[8:9], s[0:1], 0x80
	s_add_i32 s18, s87, 0x2a00
	s_mov_b32 s19, 11
	s_mov_b32 s24, 0xc3e00000
	v_mov_b32_e32 v150, 0x43e00000
	v_lshlrev_b32_e32 v146, 4, v194
	v_mul_u32_u24_e32 v147, 0x240, v194
	s_lshl_b32 s20, s93, 4
	v_add_u32_e32 v147, s20, v147
	v_lshrrev_b32_e32 v151, 3, v194
	s_lshl_b32 s20, s93, 5
	v_add_u32_e32 v152, s20, v151
	v_mul_u32_u24_e32 v148, 0x90, v152
	v_and_b32_e32 v152, 7, v194
	v_lshl_add_u32 v148, v152, 4, v148
	v_lshlrev_b32_e32 v151, 7, v151
	v_lshl_add_u32 v149, v152, 4, v151
	s_waitcnt lgkmcnt(0)
	s_cmp_lt_u32 s18, 0x2000
	s_cbranch_scc0 .Lcv4_dnP0
	s_lshr_b32 s20, s18, 4
	s_lshl_b32 s20, s20, 21
	s_and_b32 s21, s18, 15
	s_lshl_b32 s21, s21, 10
	s_add_u32 s20, s20, s21
	s_lshl_b32 s21, s93, 18
	s_add_u32 s20, s20, s21
	s_add_u32 s10, s6, s20
	s_addc_u32 s11, s7, 0
	s_movk_i32 s12, 0x4000
	s_lshl_b32 s20, s18, 15
	s_add_u32 s20, s20, 0x30000000
	s_branch .Lcv4_cmP0

; __device__ __forceinline__ Cvb conv8b_dec(const Ctx& X, int bit) { Cvb c; int kb, nb;
;     if (bit < I_GU8 / 8) { const int e = bit >> 8, r = bit & 255; kb = r >> 4; nb = r & 15; c.N = 2 * DFF; c.W = XP_w_gu(X) + (size_t)e * D * (2 * DFF); c.WT = XP_WguT(X) + (size_t)e * 16 * PAN_GU + (size_t)kb * PAN_GU; }
;     else { const int b2 = bit - I_GU8 / 8, e = b2 >> 7, r = b2 & 127; kb = r >> 3; nb = r & 7; c.N = D; c.W = XP_w_d(X) + (size_t)e * DFF * D; c.WT = XP_WdT(X) + (size_t)e * 16 * PAN_D + (size_t)kb * PAN_D; }
;     c.W += (size_t)(kb * 128 + 16 * X.wave) * c.N + nb * 256 + 4 * X.lane;
;     c.WT += (size_t)(nb * 256 + 32 * X.wave + (X.lane >> 3)) * 128 + 16 * (X.lane & 7);
;     return c; }
; __device__ __forceinline__ void conv8b_run(const Ctx& X, int first, int step, int count) {
;     if (count <= 0) return;
;     f32x4 v[16];
;     Cvb c = conv8b_dec(X, first), cn = c;
; #pragma unroll
;     for (int i = 0; i < 16; ++i) v[i] = __builtin_nontemporal_load((const f32x4*)(c.W + (size_t)i * c.N));
.Lcv4_cmP0:
	s_lshl_b32 s21, s93, 12
	s_add_u32 s20, s20, s21
	s_add_u32 s32, s90, s20
	s_addc_u32 s33, s91, 0
	global_load_dwordx4 v[2:5], v146, s[10:11] nt
	s_add_u32 s10, s10, s12
	s_addc_u32 s11, s11, 0
	global_load_dwordx4 v[6:9], v146, s[10:11] nt
	s_add_u32 s10, s10, s12
	s_addc_u32 s11, s11, 0
	global_load_dwordx4 v[10:13], v146, s[10:11] nt
	s_add_u32 s10, s10, s12
	s_addc_u32 s11, s11, 0
	global_load_dwordx4 v[14:17], v146, s[10:11] nt
	s_add_u32 s10, s10, s12
	s_addc_u32 s11, s11, 0
	global_load_dwordx4 v[18:21], v146, s[10:11] nt
	s_add_u32 s10, s10, s12
	s_addc_u32 s11, s11, 0
	global_load_dwordx4 v[22:25], v146, s[10:11] nt
	s_add_u32 s10, s10, s12
	s_addc_u32 s11, s11, 0
	global_load_dwordx4 v[26:29], v146, s[10:11] nt
	s_add_u32 s10, s10, s12
	s_addc_u32 s11, s11, 0
	global_load_dwordx4 v[30:33], v146, s[10:11] nt
	s_add_u32 s10, s10, s12
	s_addc_u32 s11, s11, 0
	global_load_dwordx4 v[34:37], v146, s[10:11] nt
	s_add_u32 s10, s10, s12
	s_addc_u32 s11, s11, 0
	global_load_dwordx4 v[38:41], v146, s[10:11] nt
	s_add_u32 s10, s10, s12
	s_addc_u32 s11, s11, 0
	global_load_dwordx4 v[42:45], v146, s[10:11] nt
	s_add_u32 s10, s10, s12
	s_addc_u32 s11, s11, 0
	global_load_dwordx4 v[46:49], v146, s[10:11] nt
	s_add_u32 s10, s10, s12
	s_addc_u32 s11, s11, 0
	global_load_dwordx4 v[50:53], v146, s[10:11] nt
	s_add_u32 s10, s10, s12
	s_addc_u32 s11, s11, 0
	global_load_dwordx4 v[54:57], v146, s[10:11] nt
	s_add_u32 s10, s10, s12
	s_addc_u32 s11, s11, 0
	global_load_dwordx4 v[58:61], v146, s[10:11] nt
	s_add_u32 s10, s10, s12
	s_addc_u32 s11, s11, 0
	global_load_dwordx4 v[62:65], v146, s[10:11] nt
	s_add_i32 s18, s18, 128
	s_add_i32 s19, s19, -1
	s_mov_b32 s25, 0
	s_cmp_eq_u32 s19, 0
	s_cbranch_scc1 .Lcv4_loop
	s_cmp_lt_u32 s18, 0x2000
	s_cbranch_scc0 .Lcv4_dnP1
	s_lshr_b32 s20, s18, 4
	s_lshl_b32 s20, s20, 21
	s_and_b32 s21, s18, 15
	s_lshl_b32 s21, s21, 10
	s_add_u32 s20, s20, s21
	s_lshl_b32 s21, s93, 18
	s_add_u32 s20, s20, s21
	s_add_u32 s10, s6, s20
	s_addc_u32 s11, s7, 0
	s_movk_i32 s12, 0x4000
	s_lshl_b32 s20, s18, 15
	s_add_u32 s20, s20, 0x30000000
	s_branch .Lcv4_cmP1

; __device__ __forceinline__ void conv8b_run(const Ctx& X, int first, int step, int count) {
;     ...
;         if (j + 1 < count) { cn = conv8b_dec(X, first + (j + 1) * step);
; #pragma unroll
;             for (int i = 0; i < 16; ++i) v[i] = __builtin_nontemporal_load((const f32x4*)(cn.W + (size_t)i * cn.N)); }
.Lcv4_cmP1:
	s_lshl_b32 s21, s93, 12
	s_add_u32 s20, s20, s21
	s_add_u32 s34, s90, s20
	s_addc_u32 s35, s91, 0
	global_load_dwordx4 v[66:69], v146, s[10:11] nt
	s_add_u32 s10, s10, s12
	s_addc_u32 s11, s11, 0
	global_load_dwordx4 v[70:73], v146, s[10:11] nt
	s_add_u32 s10, s10, s12
	s_addc_u32 s11, s11, 0
	global_load_dwordx4 v[74:77], v146, s[10:11] nt
	s_add_u32 s10, s10, s12
	s_addc_u32 s11, s11, 0
	global_load_dwordx4 v[78:81], v146, s[10:11] nt
	s_add_u32 s10, s10, s12
	s_addc_u32 s11, s11, 0
	global_load_dwordx4 v[82:85], v146, s[10:11] nt
	s_add_u32 s10, s10, s12
	s_addc_u32 s11, s11, 0
	global_load_dwordx4 v[86:89], v146, s[10:11] nt
	s_add_u32 s10, s10, s12
	s_addc_u32 s11, s11, 0
	global_load_dwordx4 v[90:93], v146, s[10:11] nt
	s_add_u32 s10, s10, s12
	s_addc_u32 s11, s11, 0
	global_load_dwordx4 v[94:97], v146, s[10:11] nt
	s_add_u32 s10, s10, s12
	s_addc_u32 s11, s11, 0
	global_load_dwordx4 v[98:101], v146, s[10:11] nt
	s_add_u32 s10, s10, s12
	s_addc_u32 s11, s11, 0
	global_load_dwordx4 v[102:105], v146, s[10:11] nt
	s_add_u32 s10, s10, s12
	s_addc_u32 s11, s11, 0
	global_load_dwordx4 v[106:109], v146, s[10:11] nt
	s_add_u32 s10, s10, s12
	s_addc_u32 s11, s11, 0
	global_load_dwordx4 v[110:113], v146, s[10:11] nt
	s_add_u32 s10, s10, s12
	s_addc_u32 s11, s11, 0
	global_load_dwordx4 v[114:117], v146, s[10:11] nt
	s_add_u32 s10, s10, s12
	s_addc_u32 s11, s11, 0
	global_load_dwordx4 v[118:121], v146, s[10:11] nt
	s_add_u32 s10, s10, s12
	s_addc_u32 s11, s11, 0
	global_load_dwordx4 v[122:125], v146, s[10:11] nt
	s_add_u32 s10, s10, s12
	s_addc_u32 s11, s11, 0
	global_load_dwordx4 v[126:129], v146, s[10:11] nt
	s_add_i32 s18, s18, 128
	s_add_i32 s19, s19, -1
	s_mov_b32 s25, 1
	s_waitcnt vmcnt(16)

; #define LAS __attribute__((address_space(3)))
; __device__ __forceinline__ void conv8b_run(const Ctx& X, int first, int step, int count) {
;     ...
;         LAS uchar* buf = X.lds + (j & 1) * CVT_BUF;
; #pragma unroll
;         for (int q = 0; q < 4; ++q) { u32x4 o;
;             o.x = pk_fp8x4(v[0][q] * W8_SCALE, v[1][q] * W8_SCALE, v[2][q] * W8_SCALE, v[3][q] * W8_SCALE); o.y = pk_fp8x4(v[4][q] * W8_SCALE, v[5][q] * W8_SCALE, v[6][q] * W8_SCALE, v[7][q] * W8_SCALE);
;             o.z = pk_fp8x4(v[8][q] * W8_SCALE, v[9][q] * W8_SCALE, v[10][q] * W8_SCALE, v[11][q] * W8_SCALE); o.w = pk_fp8x4(v[12][q] * W8_SCALE, v[13][q] * W8_SCALE, v[14][q] * W8_SCALE, v[15][q] * W8_SCALE);
;             *(LAS u32x4*)(buf + (4 * X.lane + q) * CVT_STRIDE + 16 * X.wave) = o; }
;         if (j + 1 < count) { cn = conv8b_dec(X, first + (j + 1) * step);
; #pragma unroll
;             for (int i = 0; i < 16; ++i) v[i] = __builtin_nontemporal_load((const f32x4*)(cn.W + (size_t)i * cn.N)); }
;         asm volatile("s_waitcnt lgkmcnt(0)" ::: "memory"); __builtin_amdgcn_s_barrier();
; #pragma unroll
;         for (int it = 0; it < 4; ++it) { const u32x4 r = *(const LAS u32x4*)(buf + (32 * X.wave + 8 * it + (X.lane >> 3)) * CVT_STRIDE + 16 * (X.lane & 7));
;             __builtin_nontemporal_store(r, (u32x4*)(c.WT + (size_t)it * 8 * 128)); }
.Lcv4_w1A:
	v_mul_f32_e32 v2, 0x42800000, v2
	v_mul_f32_e32 v6, 0x42800000, v6
	v_med3_f32 v2, v2, s24, v150
	v_med3_f32 v6, v6, s24, v150
	v_mul_f32_e32 v10, 0x42800000, v10
	v_mul_f32_e32 v14, 0x42800000, v14
	v_cvt_pk_fp8_f32 v130, v2, v6
	v_med3_f32 v10, v10, s24, v150
	v_med3_f32 v14, v14, s24, v150
	v_cvt_pk_fp8_f32 v130, v10, v14 op_sel:[0,0,1]
	v_mul_f32_e32 v18, 0x42800000, v18
	v_mul_f32_e32 v22, 0x42800000, v22
	v_med3_f32 v18, v18, s24, v150
	v_med3_f32 v22, v22, s24, v150
	v_mul_f32_e32 v26, 0x42800000, v26
	v_mul_f32_e32 v30, 0x42800000, v30
	v_cvt_pk_fp8_f32 v131, v18, v22
	v_med3_f32 v26, v26, s24, v150
	v_med3_f32 v30, v30, s24, v150
	v_cvt_pk_fp8_f32 v131, v26, v30 op_sel:[0,0,1]
	v_mul_f32_e32 v34, 0x42800000, v34
	v_mul_f32_e32 v38, 0x42800000, v38
	v_med3_f32 v34, v34, s24, v150
	v_med3_f32 v38, v38, s24, v150
	v_mul_f32_e32 v42, 0x42800000, v42
	v_mul_f32_e32 v46, 0x42800000, v46
	v_cvt_pk_fp8_f32 v132, v34, v38
	v_med3_f32 v42, v42, s24, v150
	v_med3_f32 v46, v46, s24, v150
	v_cvt_pk_fp8_f32 v132, v42, v46 op_sel:[0,0,1]
	v_mul_f32_e32 v50, 0x42800000, v50
	v_mul_f32_e32 v54, 0x42800000, v54
	v_med3_f32 v50, v50, s24, v150
	v_med3_f32 v54, v54, s24, v150
	v_mul_f32_e32 v58, 0x42800000, v58
	v_mul_f32_e32 v62, 0x42800000, v62
	v_cvt_pk_fp8_f32 v133, v50, v54
	v_med3_f32 v58, v58, s24, v150
	v_med3_f32 v62, v62, s24, v150
	v_cvt_pk_fp8_f32 v133, v58, v62 op_sel:[0,0,1]
	s_nop 0
	ds_write_b128 v147, v[130:133] offset:0
	v_mul_f32_e32 v3, 0x42800000, v3
	v_mul_f32_e32 v7, 0x42800000, v7
	v_med3_f32 v3, v3, s24, v150
	v_med3_f32 v7, v7, s24, v150
	v_mul_f32_e32 v11, 0x42800000, v11
	v_mul_f32_e32 v15, 0x42800000, v15
	v_cvt_pk_fp8_f32 v134, v3, v7
	v_med3_f32 v11, v11, s24, v150
	v_med3_f32 v15, v15, s24, v150
	v_cvt_pk_fp8_f32 v134, v11, v15 op_sel:[0,0,1]
	v_mul_f32_e32 v19, 0x42800000, v19
	v_mul_f32_e32 v23, 0x42800000, v23
	v_med3_f32 v19, v19, s24, v150
	v_med3_f32 v23, v23, s24, v150
	v_mul_f32_e32 v27, 0x42800000, v27
	v_mul_f32_e32 v31, 0x42800000, v31
	v_cvt_pk_fp8_f32 v135, v19, v23
	v_med3_f32 v27, v27, s24, v150
	v_med3_f32 v31, v31, s24, v150
	v_cvt_pk_fp8_f32 v135, v27, v31 op_sel:[0,0,1]
	v_mul_f32_e32 v35, 0x42800000, v35
	v_mul_f32_e32 v39, 0x42800000, v39
	v_med3_f32 v35, v35, s24, v150
	v_med3_f32 v39, v39, s24, v150
	v_mul_f32_e32 v43, 0x42800000, v43
	v_mul_f32_e32 v47, 0x42800000, v47
	v_cvt_pk_fp8_f32 v136, v35, v39
	v_med3_f32 v43, v43, s24, v150
	v_med3_f32 v47, v47, s24, v150
	v_cvt_pk_fp8_f32 v136, v43, v47 op_sel:[0,0,1]
	v_mul_f32_e32 v51, 0x42800000, v51
	v_mul_f32_e32 v55, 0x42800000, v55
	v_med3_f32 v51, v51, s24, v150
	v_med3_f32 v55, v55, s24, v150
	v_mul_f32_e32 v59, 0x42800000, v59
	v_mul_f32_e32 v63, 0x42800000, v63
	v_cvt_pk_fp8_f32 v137, v51, v55
	v_med3_f32 v59, v59, s24, v150
	v_med3_f32 v63, v63, s24, v150
	v_cvt_pk_fp8_f32 v137, v59, v63 op_sel:[0,0,1]
	s_nop 0
	ds_write_b128 v147, v[134:137] offset:144
	v_mul_f32_e32 v4, 0x42800000, v4
	v_mul_f32_e32 v8, 0x42800000, v8
	v_med3_f32 v4, v4, s24, v150
	v_med3_f32 v8, v8, s24, v150
	v_mul_f32_e32 v12, 0x42800000, v12
	v_mul_f32_e32 v16, 0x42800000, v16
	v_cvt_pk_fp8_f32 v138, v4, v8
	v_med3_f32 v12, v12, s24, v150
	v_med3_f32 v16, v16, s24, v150
	v_cvt_pk_fp8_f32 v138, v12, v16 op_sel:[0,0,1]
	v_mul_f32_e32 v20, 0x42800000, v20
	v_mul_f32_e32 v24, 0x42800000, v24
	v_med3_f32 v20, v20, s24, v150
	v_med3_f32 v24, v24, s24, v150
	v_mul_f32_e32 v28, 0x42800000, v28
	v_mul_f32_e32 v32, 0x42800000, v32
	v_cvt_pk_fp8_f32 v139, v20, v24
	v_med3_f32 v28, v28, s24, v150
	v_med3_f32 v32, v32, s24, v150
	v_cvt_pk_fp8_f32 v139, v28, v32 op_sel:[0,0,1]
	v_mul_f32_e32 v36, 0x42800000, v36
	v_mul_f32_e32 v40, 0x42800000, v40
	v_med3_f32 v36, v36, s24, v150
	v_med3_f32 v40, v40, s24, v150
	v_mul_f32_e32 v44, 0x42800000, v44
	v_mul_f32_e32 v48, 0x42800000, v48
	v_cvt_pk_fp8_f32 v140, v36, v40
	v_med3_f32 v44, v44, s24, v150
	v_med3_f32 v48, v48, s24, v150
	v_cvt_pk_fp8_f32 v140, v44, v48 op_sel:[0,0,1]
	v_mul_f32_e32 v52, 0x42800000, v52
	v_mul_f32_e32 v56, 0x42800000, v56
	v_med3_f32 v52, v52, s24, v150
	v_med3_f32 v56, v56, s24, v150
	v_mul_f32_e32 v60, 0x42800000, v60
	v_mul_f32_e32 v64, 0x42800000, v64
	v_cvt_pk_fp8_f32 v141, v52, v56
	v_med3_f32 v60, v60, s24, v150
	v_med3_f32 v64, v64, s24, v150
	v_cvt_pk_fp8_f32 v141, v60, v64 op_sel:[0,0,1]
	s_nop 0
	ds_write_b128 v147, v[138:141] offset:288
	v_mul_f32_e32 v5, 0x42800000, v5
	v_mul_f32_e32 v9, 0x42800000, v9
	v_med3_f32 v5, v5, s24, v150
	v_med3_f32 v9, v9, s24, v150
	v_mul_f32_e32 v13, 0x42800000, v13
	v_mul_f32_e32 v17, 0x42800000, v17
	v_cvt_pk_fp8_f32 v142, v5, v9
	v_med3_f32 v13, v13, s24, v150
	v_med3_f32 v17, v17, s24, v150
	v_cvt_pk_fp8_f32 v142, v13, v17 op_sel:[0,0,1]
	v_mul_f32_e32 v21, 0x42800000, v21
	v_mul_f32_e32 v25, 0x42800000, v25
	v_med3_f32 v21, v21, s24, v150
	v_med3_f32 v25, v25, s24, v150
	v_mul_f32_e32 v29, 0x42800000, v29
	v_mul_f32_e32 v33, 0x42800000, v33
	v_cvt_pk_fp8_f32 v143, v21, v25
	v_med3_f32 v29, v29, s24, v150
	v_med3_f32 v33, v33, s24, v150
	v_cvt_pk_fp8_f32 v143, v29, v33 op_sel:[0,0,1]
	v_mul_f32_e32 v37, 0x42800000, v37
	v_mul_f32_e32 v41, 0x42800000, v41
	v_med3_f32 v37, v37, s24, v150
	v_med3_f32 v41, v41, s24, v150
	v_mul_f32_e32 v45, 0x42800000, v45
	v_mul_f32_e32 v49, 0x42800000, v49
	v_cvt_pk_fp8_f32 v144, v37, v41
	v_med3_f32 v45, v45, s24, v150
	v_med3_f32 v49, v49, s24, v150
	v_cvt_pk_fp8_f32 v144, v45, v49 op_sel:[0,0,1]
	v_mul_f32_e32 v53, 0x42800000, v53
	v_mul_f32_e32 v57, 0x42800000, v57
	v_med3_f32 v53, v53, s24, v150
	v_med3_f32 v57, v57, s24, v150
	v_mul_f32_e32 v61, 0x42800000, v61
	v_mul_f32_e32 v65, 0x42800000, v65
	v_cvt_pk_fp8_f32 v145, v53, v57
	v_med3_f32 v61, v61, s24, v150
	v_med3_f32 v65, v65, s24, v150
	v_cvt_pk_fp8_f32 v145, v61, v65 op_sel:[0,0,1]
	s_nop 0
	ds_write_b128 v147, v[142:145] offset:432
	s_waitcnt lgkmcnt(0)
	s_barrier
	ds_read_b128 v[130:133], v148 offset:0
	ds_read_b128 v[134:137], v148 offset:1152
	ds_read_b128 v[138:141], v148 offset:2304
	ds_read_b128 v[142:145], v148 offset:3456
	s_waitcnt lgkmcnt(3)
	global_store_dwordx4 v149, v[130:133], s[32:33] nt
	s_waitcnt lgkmcnt(2)
	global_store_dwordx4 v149, v[134:137], s[32:33] offset:1024 nt
	s_waitcnt lgkmcnt(1)
	global_store_dwordx4 v149, v[138:141], s[32:33] offset:2048 nt
	s_waitcnt lgkmcnt(0)
	global_store_dwordx4 v149, v[142:145], s[32:33] offset:3072 nt
	s_cmp_eq_u32 s25, 0
	s_cbranch_scc1 .Lcv4_done
	s_cmp_eq_u32 s19, 0
	s_cbranch_scc1 .Lcv4_nlA
	s_cmp_lt_u32 s18, 0x2000
	s_cbranch_scc0 .Lcv4_dnLA
	s_lshr_b32 s20, s18, 4
	s_lshl_b32 s20, s20, 21
	s_and_b32 s21, s18, 15
	s_lshl_b32 s21, s21, 10
	s_add_u32 s20, s20, s21
	s_lshl_b32 s21, s93, 18
	s_add_u32 s20, s20, s21
	s_add_u32 s10, s6, s20
	s_addc_u32 s11, s7, 0
	s_movk_i32 s12, 0x4000
	s_lshl_b32 s20, s18, 15
	s_add_u32 s20, s20, 0x30000000
	s_branch .Lcv4_cmLA

; __device__ __forceinline__ void conv8b_run(const Ctx& X, int first, int step, int count) {
;     ...
;         if (j + 1 < count) { cn = conv8b_dec(X, first + (j + 1) * step);
; #pragma unroll
;             for (int i = 0; i < 16; ++i) v[i] = __builtin_nontemporal_load((const f32x4*)(cn.W + (size_t)i * cn.N)); }
.Lcv4_cmLA:
	s_lshl_b32 s21, s93, 12
	s_add_u32 s20, s20, s21
	s_add_u32 s32, s90, s20
	s_addc_u32 s33, s91, 0
	global_load_dwordx4 v[2:5], v146, s[10:11] nt
	s_add_u32 s10, s10, s12
	s_addc_u32 s11, s11, 0
	global_load_dwordx4 v[6:9], v146, s[10:11] nt
	s_add_u32 s10, s10, s12
	s_addc_u32 s11, s11, 0
	global_load_dwordx4 v[10:13], v146, s[10:11] nt
	s_add_u32 s10, s10, s12
	s_addc_u32 s11, s11, 0
	global_load_dwordx4 v[14:17], v146, s[10:11] nt
	s_add_u32 s10, s10, s12
	s_addc_u32 s11, s11, 0
	global_load_dwordx4 v[18:21], v146, s[10:11] nt
	s_add_u32 s10, s10, s12
	s_addc_u32 s11, s11, 0
	global_load_dwordx4 v[22:25], v146, s[10:11] nt
	s_add_u32 s10, s10, s12
	s_addc_u32 s11, s11, 0
	global_load_dwordx4 v[26:29], v146, s[10:11] nt
	s_add_u32 s10, s10, s12
	s_addc_u32 s11, s11, 0
	global_load_dwordx4 v[30:33], v146, s[10:11] nt
	s_add_u32 s10, s10, s12
	s_addc_u32 s11, s11, 0
	global_load_dwordx4 v[34:37], v146, s[10:11] nt
	s_add_u32 s10, s10, s12
	s_addc_u32 s11, s11, 0
	global_load_dwordx4 v[38:41], v146, s[10:11] nt
	s_add_u32 s10, s10, s12
	s_addc_u32 s11, s11, 0
	global_load_dwordx4 v[42:45], v146, s[10:11] nt
	s_add_u32 s10, s10, s12
	s_addc_u32 s11, s11, 0
	global_load_dwordx4 v[46:49], v146, s[10:11] nt
	s_add_u32 s10, s10, s12
	s_addc_u32 s11, s11, 0
	global_load_dwordx4 v[50:53], v146, s[10:11] nt
	s_add_u32 s10, s10, s12
	s_addc_u32 s11, s11, 0
	global_load_dwordx4 v[54:57], v146, s[10:11] nt
	s_add_u32 s10, s10, s12
	s_addc_u32 s11, s11, 0
	global_load_dwordx4 v[58:61], v146, s[10:11] nt
	s_add_u32 s10, s10, s12
	s_addc_u32 s11, s11, 0
	global_load_dwordx4 v[62:65], v146, s[10:11] nt
	s_add_i32 s18, s18, 128
	s_add_i32 s19, s19, -1
	s_branch .Lcv4_nxA

; #define LAS __attribute__((address_space(3)))
; __device__ __forceinline__ void conv8b_run(const Ctx& X, int first, int step, int count) {
;     ...
;         LAS uchar* buf = X.lds + (j & 1) * CVT_BUF;
; #pragma unroll
;         for (int q = 0; q < 4; ++q) { u32x4 o;
;             o.x = pk_fp8x4(v[0][q] * W8_SCALE, v[1][q] * W8_SCALE, v[2][q] * W8_SCALE, v[3][q] * W8_SCALE); o.y = pk_fp8x4(v[4][q] * W8_SCALE, v[5][q] * W8_SCALE, v[6][q] * W8_SCALE, v[7][q] * W8_SCALE);
;             o.z = pk_fp8x4(v[8][q] * W8_SCALE, v[9][q] * W8_SCALE, v[10][q] * W8_SCALE, v[11][q] * W8_SCALE); o.w = pk_fp8x4(v[12][q] * W8_SCALE, v[13][q] * W8_SCALE, v[14][q] * W8_SCALE, v[15][q] * W8_SCALE);
;             *(LAS u32x4*)(buf + (4 * X.lane + q) * CVT_STRIDE + 16 * X.wave) = o; }
;         if (j + 1 < count) { cn = conv8b_dec(X, first + (j + 1) * step);
; #pragma unroll
;             for (int i = 0; i < 16; ++i) v[i] = __builtin_nontemporal_load((const f32x4*)(cn.W + (size_t)i * cn.N)); }
;         asm volatile("s_waitcnt lgkmcnt(0)" ::: "memory"); __builtin_amdgcn_s_barrier();
; #pragma unroll
;         for (int it = 0; it < 4; ++it) { const u32x4 r = *(const LAS u32x4*)(buf + (32 * X.wave + 8 * it + (X.lane >> 3)) * CVT_STRIDE + 16 * (X.lane & 7));
;             __builtin_nontemporal_store(r, (u32x4*)(c.WT + (size_t)it * 8 * 128)); }
;         c = cn;
.Lcv4_w1B:
	v_mul_f32_e32 v66, 0x42800000, v66
	v_mul_f32_e32 v70, 0x42800000, v70
	v_med3_f32 v66, v66, s24, v150
	v_med3_f32 v70, v70, s24, v150
	v_mul_f32_e32 v74, 0x42800000, v74
	v_mul_f32_e32 v78, 0x42800000, v78
	v_cvt_pk_fp8_f32 v130, v66, v70
	v_med3_f32 v74, v74, s24, v150
	v_med3_f32 v78, v78, s24, v150
	v_cvt_pk_fp8_f32 v130, v74, v78 op_sel:[0,0,1]
	v_mul_f32_e32 v82, 0x42800000, v82
	v_mul_f32_e32 v86, 0x42800000, v86
	v_med3_f32 v82, v82, s24, v150
	v_med3_f32 v86, v86, s24, v150
	v_mul_f32_e32 v90, 0x42800000, v90
	v_mul_f32_e32 v94, 0x42800000, v94
	v_cvt_pk_fp8_f32 v131, v82, v86
	v_med3_f32 v90, v90, s24, v150
	v_med3_f32 v94, v94, s24, v150
	v_cvt_pk_fp8_f32 v131, v90, v94 op_sel:[0,0,1]
	v_mul_f32_e32 v98, 0x42800000, v98
	v_mul_f32_e32 v102, 0x42800000, v102
	v_med3_f32 v98, v98, s24, v150
	v_med3_f32 v102, v102, s24, v150
	v_mul_f32_e32 v106, 0x42800000, v106
	v_mul_f32_e32 v110, 0x42800000, v110
	v_cvt_pk_fp8_f32 v132, v98, v102
	v_med3_f32 v106, v106, s24, v150
	v_med3_f32 v110, v110, s24, v150
	v_cvt_pk_fp8_f32 v132, v106, v110 op_sel:[0,0,1]
	v_mul_f32_e32 v114, 0x42800000, v114
	v_mul_f32_e32 v118, 0x42800000, v118
	v_med3_f32 v114, v114, s24, v150
	v_med3_f32 v118, v118, s24, v150
	v_mul_f32_e32 v122, 0x42800000, v122
	v_mul_f32_e32 v126, 0x42800000, v126
	v_cvt_pk_fp8_f32 v133, v114, v118
	v_med3_f32 v122, v122, s24, v150
	v_med3_f32 v126, v126, s24, v150
	v_cvt_pk_fp8_f32 v133, v122, v126 op_sel:[0,0,1]
	s_nop 0
	ds_write_b128 v147, v[130:133] offset:36864
	v_mul_f32_e32 v67, 0x42800000, v67
	v_mul_f32_e32 v71, 0x42800000, v71
	v_med3_f32 v67, v67, s24, v150
	v_med3_f32 v71, v71, s24, v150
	v_mul_f32_e32 v75, 0x42800000, v75
	v_mul_f32_e32 v79, 0x42800000, v79
	v_cvt_pk_fp8_f32 v134, v67, v71
	v_med3_f32 v75, v75, s24, v150
	v_med3_f32 v79, v79, s24, v150
	v_cvt_pk_fp8_f32 v134, v75, v79 op_sel:[0,0,1]
	v_mul_f32_e32 v83, 0x42800000, v83
	v_mul_f32_e32 v87, 0x42800000, v87
	v_med3_f32 v83, v83, s24, v150
	v_med3_f32 v87, v87, s24, v150
	v_mul_f32_e32 v91, 0x42800000, v91
	v_mul_f32_e32 v95, 0x42800000, v95
	v_cvt_pk_fp8_f32 v135, v83, v87
	v_med3_f32 v91, v91, s24, v150
	v_med3_f32 v95, v95, s24, v150
	v_cvt_pk_fp8_f32 v135, v91, v95 op_sel:[0,0,1]
	v_mul_f32_e32 v99, 0x42800000, v99
	v_mul_f32_e32 v103, 0x42800000, v103
	v_med3_f32 v99, v99, s24, v150
	v_med3_f32 v103, v103, s24, v150
	v_mul_f32_e32 v107, 0x42800000, v107
	v_mul_f32_e32 v111, 0x42800000, v111
	v_cvt_pk_fp8_f32 v136, v99, v103
	v_med3_f32 v107, v107, s24, v150
	v_med3_f32 v111, v111, s24, v150
	v_cvt_pk_fp8_f32 v136, v107, v111 op_sel:[0,0,1]
	v_mul_f32_e32 v115, 0x42800000, v115
	v_mul_f32_e32 v119, 0x42800000, v119
	v_med3_f32 v115, v115, s24, v150
	v_med3_f32 v119, v119, s24, v150
	v_mul_f32_e32 v123, 0x42800000, v123
	v_mul_f32_e32 v127, 0x42800000, v127
	v_cvt_pk_fp8_f32 v137, v115, v119
	v_med3_f32 v123, v123, s24, v150
	v_med3_f32 v127, v127, s24, v150
	v_cvt_pk_fp8_f32 v137, v123, v127 op_sel:[0,0,1]
	s_nop 0
	ds_write_b128 v147, v[134:137] offset:37008
	v_mul_f32_e32 v68, 0x42800000, v68
	v_mul_f32_e32 v72, 0x42800000, v72
	v_med3_f32 v68, v68, s24, v150
	v_med3_f32 v72, v72, s24, v150
	v_mul_f32_e32 v76, 0x42800000, v76
	v_mul_f32_e32 v80, 0x42800000, v80
	v_cvt_pk_fp8_f32 v138, v68, v72
	v_med3_f32 v76, v76, s24, v150
	v_med3_f32 v80, v80, s24, v150
	v_cvt_pk_fp8_f32 v138, v76, v80 op_sel:[0,0,1]
	v_mul_f32_e32 v84, 0x42800000, v84
	v_mul_f32_e32 v88, 0x42800000, v88
	v_med3_f32 v84, v84, s24, v150
	v_med3_f32 v88, v88, s24, v150
	v_mul_f32_e32 v92, 0x42800000, v92
	v_mul_f32_e32 v96, 0x42800000, v96
	v_cvt_pk_fp8_f32 v139, v84, v88
	v_med3_f32 v92, v92, s24, v150
	v_med3_f32 v96, v96, s24, v150
	v_cvt_pk_fp8_f32 v139, v92, v96 op_sel:[0,0,1]
	v_mul_f32_e32 v100, 0x42800000, v100
	v_mul_f32_e32 v104, 0x42800000, v104
	v_med3_f32 v100, v100, s24, v150
	v_med3_f32 v104, v104, s24, v150
	v_mul_f32_e32 v108, 0x42800000, v108
	v_mul_f32_e32 v112, 0x42800000, v112
	v_cvt_pk_fp8_f32 v140, v100, v104
	v_med3_f32 v108, v108, s24, v150
	v_med3_f32 v112, v112, s24, v150
	v_cvt_pk_fp8_f32 v140, v108, v112 op_sel:[0,0,1]
	v_mul_f32_e32 v116, 0x42800000, v116
	v_mul_f32_e32 v120, 0x42800000, v120
	v_med3_f32 v116, v116, s24, v150
	v_med3_f32 v120, v120, s24, v150
	v_mul_f32_e32 v124, 0x42800000, v124
	v_mul_f32_e32 v128, 0x42800000, v128
	v_cvt_pk_fp8_f32 v141, v116, v120
	v_med3_f32 v124, v124, s24, v150
	v_med3_f32 v128, v128, s24, v150
	v_cvt_pk_fp8_f32 v141, v124, v128 op_sel:[0,0,1]
	s_nop 0
	ds_write_b128 v147, v[138:141] offset:37152
	v_mul_f32_e32 v69, 0x42800000, v69
	v_mul_f32_e32 v73, 0x42800000, v73
	v_med3_f32 v69, v69, s24, v150
	v_med3_f32 v73, v73, s24, v150
	v_mul_f32_e32 v77, 0x42800000, v77
	v_mul_f32_e32 v81, 0x42800000, v81
	v_cvt_pk_fp8_f32 v142, v69, v73
	v_med3_f32 v77, v77, s24, v150
	v_med3_f32 v81, v81, s24, v150
	v_cvt_pk_fp8_f32 v142, v77, v81 op_sel:[0,0,1]
	v_mul_f32_e32 v85, 0x42800000, v85
	v_mul_f32_e32 v89, 0x42800000, v89
	v_med3_f32 v85, v85, s24, v150
	v_med3_f32 v89, v89, s24, v150
	v_mul_f32_e32 v93, 0x42800000, v93
	v_mul_f32_e32 v97, 0x42800000, v97
	v_cvt_pk_fp8_f32 v143, v85, v89
	v_med3_f32 v93, v93, s24, v150
	v_med3_f32 v97, v97, s24, v150
	v_cvt_pk_fp8_f32 v143, v93, v97 op_sel:[0,0,1]
	v_mul_f32_e32 v101, 0x42800000, v101
	v_mul_f32_e32 v105, 0x42800000, v105
	v_med3_f32 v101, v101, s24, v150
	v_med3_f32 v105, v105, s24, v150
	v_mul_f32_e32 v109, 0x42800000, v109
	v_mul_f32_e32 v113, 0x42800000, v113
	v_cvt_pk_fp8_f32 v144, v101, v105
	v_med3_f32 v109, v109, s24, v150
	v_med3_f32 v113, v113, s24, v150
	v_cvt_pk_fp8_f32 v144, v109, v113 op_sel:[0,0,1]
	v_mul_f32_e32 v117, 0x42800000, v117
	v_mul_f32_e32 v121, 0x42800000, v121
	v_med3_f32 v117, v117, s24, v150
	v_med3_f32 v121, v121, s24, v150
	v_mul_f32_e32 v125, 0x42800000, v125
	v_mul_f32_e32 v129, 0x42800000, v129
	v_cvt_pk_fp8_f32 v145, v117, v121
	v_med3_f32 v125, v125, s24, v150
	v_med3_f32 v129, v129, s24, v150
	v_cvt_pk_fp8_f32 v145, v125, v129 op_sel:[0,0,1]
	s_nop 0
	ds_write_b128 v147, v[142:145] offset:37296
	s_waitcnt lgkmcnt(0)
	s_barrier
	ds_read_b128 v[130:133], v148 offset:36864
	ds_read_b128 v[134:137], v148 offset:38016
	ds_read_b128 v[138:141], v148 offset:39168
	ds_read_b128 v[142:145], v148 offset:40320
	s_waitcnt lgkmcnt(3)
	global_store_dwordx4 v149, v[130:133], s[34:35] nt
	s_waitcnt lgkmcnt(2)
	global_store_dwordx4 v149, v[134:137], s[34:35] offset:1024 nt
	s_waitcnt lgkmcnt(1)
	global_store_dwordx4 v149, v[138:141], s[34:35] offset:2048 nt
	s_waitcnt lgkmcnt(0)
	global_store_dwordx4 v149, v[142:145], s[34:35] offset:3072 nt
	s_cmp_eq_u32 s25, 0
	s_cbranch_scc1 .Lcv4_done
	s_cmp_eq_u32 s19, 0
	s_cbranch_scc1 .Lcv4_nlB
	s_cmp_lt_u32 s18, 0x2000
	s_cbranch_scc0 .Lcv4_dnLB
	s_lshr_b32 s20, s18, 4
	s_lshl_b32 s20, s20, 21
	s_and_b32 s21, s18, 15
	s_lshl_b32 s21, s21, 10
	s_add_u32 s20, s20, s21
	s_lshl_b32 s21, s93, 18
	s_add_u32 s20, s20, s21
	s_add_u32 s10, s6, s20
	s_addc_u32 s11, s7, 0
	s_movk_i32 s12, 0x4000
	s_lshl_b32 s20, s18, 15
	s_add_u32 s20, s20, 0x30000000
	s_branch .Lcv4_cmLB

; __device__ __forceinline__ void conv8b_run(const Ctx& X, int first, int step, int count) {
;     ...
;         if (j + 1 < count) { cn = conv8b_dec(X, first + (j + 1) * step);
; #pragma unroll
;             for (int i = 0; i < 16; ++i) v[i] = __builtin_nontemporal_load((const f32x4*)(cn.W + (size_t)i * cn.N)); }
.Lcv4_cmLB:
	s_lshl_b32 s21, s93, 12
	s_add_u32 s20, s20, s21
	s_add_u32 s34, s90, s20
	s_addc_u32 s35, s91, 0
	global_load_dwordx4 v[66:69], v146, s[10:11] nt
	s_add_u32 s10, s10, s12
	s_addc_u32 s11, s11, 0
	global_load_dwordx4 v[70:73], v146, s[10:11] nt
	s_add_u32 s10, s10, s12
	s_addc_u32 s11, s11, 0
	global_load_dwordx4 v[74:77], v146, s[10:11] nt
	s_add_u32 s10, s10, s12
	s_addc_u32 s11, s11, 0
	global_load_dwordx4 v[78:81], v146, s[10:11] nt
	s_add_u32 s10, s10, s12
	s_addc_u32 s11, s11, 0
	global_load_dwordx4 v[82:85], v146, s[10:11] nt
	s_add_u32 s10, s10, s12
	s_addc_u32 s11, s11, 0
	global_load_dwordx4 v[86:89], v146, s[10:11] nt
	s_add_u32 s10, s10, s12
	s_addc_u32 s11, s11, 0
	global_load_dwordx4 v[90:93], v146, s[10:11] nt
	s_add_u32 s10, s10, s12
	s_addc_u32 s11, s11, 0
	global_load_dwordx4 v[94:97], v146, s[10:11] nt
	s_add_u32 s10, s10, s12
	s_addc_u32 s11, s11, 0
	global_load_dwordx4 v[98:101], v146, s[10:11] nt
	s_add_u32 s10, s10, s12
	s_addc_u32 s11, s11, 0
	global_load_dwordx4 v[102:105], v146, s[10:11] nt
	s_add_u32 s10, s10, s12
	s_addc_u32 s11, s11, 0
	global_load_dwordx4 v[106:109], v146, s[10:11] nt
	s_add_u32 s10, s10, s12
	s_addc_u32 s11, s11, 0
	global_load_dwordx4 v[110:113], v146, s[10:11] nt
	s_add_u32 s10, s10, s12
	s_addc_u32 s11, s11, 0
	global_load_dwordx4 v[114:117], v146, s[10:11] nt
	s_add_u32 s10, s10, s12
	s_addc_u32 s11, s11, 0
	global_load_dwordx4 v[118:121], v146, s[10:11] nt
	s_add_u32 s10, s10, s12
	s_addc_u32 s11, s11, 0
	global_load_dwordx4 v[122:125], v146, s[10:11] nt
	s_add_u32 s10, s10, s12
	s_addc_u32 s11, s11, 0
	global_load_dwordx4 v[126:129], v146, s[10:11] nt
	s_add_i32 s18, s18, 128
	s_add_i32 s19, s19, -1
	s_branch .Lcv4_nxB
